# prep: magic-number int8 quantize, second-round tiles spread over all blocks, b1 and weight-image loads hoisted to kernel start
# baseline (speedup 1.0000x reference)
_Z4prepPKfS0_S0_S0_S0_Pc:
	v_lshrrev_b32_e32 v69, 7, v0
	v_bfe_u32 v1, v0, 6, 1
	v_lshl_or_b32 v128, s2, 2, v69
	s_lshl_b32 s32, s2, 1
	s_addk_i32 s32, 0x400
	v_add_u32_e32 v183, s32, v69
	s_add_u32 s33, s2, 0x600
	s_cmp_lt_u32 s2, 27
	s_cselect_b32 s33, s33, 0x7fff
	v_mov_b32_e32 v184, 0x7fff
	v_mov_b32_e32 v185, s33
	v_cmp_eq_u32_e32 vcc, 2, v69
	s_nop 1
	v_cndmask_b32_e32 v184, v184, v185, vcc
	v_cmp_gt_u32_e32 vcc, 2, v69
	s_nop 1
	v_cndmask_b32_e32 v183, v184, v183, vcc
	v_cmp_eq_u32_e32 vcc, 1, v1
	s_nop 1
	v_cndmask_b32_e32 v2, v128, v183, vcc
	s_load_dwordx8 s[4:11], s[0:1], 0x0
	s_load_dwordx2 s[16:17], s[0:1], 0x28
	s_load_dwordx2 s[36:37], s[0:1], 0x20
	v_min_i32_e32 v2, 0x61a, v2
	v_bfe_u32 v68, v0, 5, 1
	v_lshl_or_b32 v104, v2, 5, v68
	v_lshlrev_b32_e32 v2, 2, v0
	v_and_b32_e32 v129, 0x7c, v2
	v_min_i32_e32 v2, 0xc34f, v104
	v_lshlrev_b32_e32 v58, 2, v129
	v_mov_b32_e32 v59, 0
	v_ashrrev_i32_e32 v3, 31, v2
	s_waitcnt lgkmcnt(0)
	s_cmp_gt_u32 s2, 17
	s_cbranch_scc1 .Lmy_img_skip
	v_lshl_or_b32 v192, s2, 9, v0
	v_ashrrev_i32_e32 v193, 7, v192
	v_lshlrev_b32_e32 v194, 1, v193
	v_lshlrev_b32_e32 v195, 3, v193
	v_and_b32_e32 v195, 16, v195
	v_and_b32_e32 v196, 12, v193
	v_and_b32_e32 v197, 0xffffffe2, v194
	v_or3_b32 v197, v195, v196, v197
	v_cmp_gt_i32_e32 vcc, 64, v193
	s_nop 1
	v_cndmask_b32_e32 v198, v194, v197, vcc
	v_and_b32_e32 v199, 0x7f, v0
	v_lshl_or_b32 v198, v198, 7, v199
	v_add_u32_e32 v200, 0x8000, v198
	v_mov_b32_e32 v201, 0
	v_lshl_add_u64 v[200:201], v[200:201], 2, s[6:7]
	global_load_dword v188, v[200:201], off
	global_load_dword v189, v[200:201], off offset:512
	v_lshl_or_b32 v202, v197, 7, v199
	v_mov_b32_e32 v203, 0
	v_lshl_add_u64 v[202:203], v[202:203], 2, s[10:11]
	s_cmp_gt_u32 s2, 15
	s_cbranch_scc1 .Lmy_img_skip
	global_load_dword v190, v[202:203], off
	global_load_dword v191, v[202:203], off offset:512
	s_cmp_lg_u32 s2, 0
	s_cbranch_scc1 .Lmy_img_skip
	v_lshlrev_b32_e32 v204, 2, v199
	global_load_dword v187, v204, s[36:37]
.Lmy_img_skip:
	v_lshlrev_b32_e32 v186, 3, v0
	v_and_b32_e32 v186, 0x100, v186
	global_load_dwordx4 v[192:195], v186, s[8:9]
	global_load_dwordx4 v[196:199], v186, s[8:9] offset:16
	global_load_dwordx4 v[200:203], v186, s[8:9] offset:32
	global_load_dwordx4 v[204:207], v186, s[8:9] offset:48
	global_load_dwordx4 v[208:211], v186, s[8:9] offset:64
	global_load_dwordx4 v[212:215], v186, s[8:9] offset:80
	global_load_dwordx4 v[216:219], v186, s[8:9] offset:96
	global_load_dwordx4 v[220:223], v186, s[8:9] offset:112
	global_load_dwordx4 v[224:227], v186, s[8:9] offset:128
	global_load_dwordx4 v[228:231], v186, s[8:9] offset:144
	global_load_dwordx4 v[232:235], v186, s[8:9] offset:160
	global_load_dwordx4 v[236:239], v186, s[8:9] offset:176
	global_load_dwordx4 v[240:243], v186, s[8:9] offset:192
	global_load_dwordx4 v[244:247], v186, s[8:9] offset:208
	global_load_dwordx4 v[248:251], v186, s[8:9] offset:224
	global_load_dwordx4 v[252:255], v186, s[8:9] offset:240
	v_lshl_add_u64 v[60:61], s[4:5], 0, v[58:59]
	v_lshlrev_b64 v[2:3], 9, v[2:3]
	v_lshl_add_u64 v[10:11], v[60:61], 0, v[2:3]
	v_or_b32_e32 v2, 2, v104
	v_min_i32_e32 v2, 0xc34f, v2
	v_ashrrev_i32_e32 v3, 31, v2
	v_lshlrev_b64 v[2:3], 9, v[2:3]
	v_lshl_add_u64 v[12:13], v[60:61], 0, v[2:3]
	global_load_dwordx4 v[6:9], v[10:11], off nt
	global_load_dwordx4 v[2:5], v[12:13], off nt
	v_or_b32_e32 v10, 4, v104
	v_min_i32_e32 v10, 0xc34f, v10
	v_ashrrev_i32_e32 v11, 31, v10
	v_lshlrev_b64 v[10:11], 9, v[10:11]
	v_lshl_add_u64 v[18:19], v[60:61], 0, v[10:11]
	v_or_b32_e32 v10, 6, v104
	v_min_i32_e32 v10, 0xc34f, v10
	v_ashrrev_i32_e32 v11, 31, v10
	v_lshlrev_b64 v[10:11], 9, v[10:11]
	v_lshl_add_u64 v[20:21], v[60:61], 0, v[10:11]
	global_load_dwordx4 v[14:17], v[18:19], off nt
	global_load_dwordx4 v[10:13], v[20:21], off nt
	v_or_b32_e32 v18, 8, v104
	v_min_i32_e32 v18, 0xc34f, v18
	v_ashrrev_i32_e32 v19, 31, v18
	v_lshlrev_b64 v[18:19], 9, v[18:19]
	v_lshl_add_u64 v[26:27], v[60:61], 0, v[18:19]
	v_or_b32_e32 v18, 10, v104
	v_min_i32_e32 v18, 0xc34f, v18
	v_ashrrev_i32_e32 v19, 31, v18
	v_lshlrev_b64 v[18:19], 9, v[18:19]
	v_lshl_add_u64 v[28:29], v[60:61], 0, v[18:19]
	global_load_dwordx4 v[22:25], v[26:27], off nt
	global_load_dwordx4 v[18:21], v[28:29], off nt
	v_or_b32_e32 v26, 12, v104
	v_min_i32_e32 v26, 0xc34f, v26
	v_ashrrev_i32_e32 v27, 31, v26
	v_lshlrev_b32_e32 v130, 7, v0
	v_lshlrev_b64 v[26:27], 9, v[26:27]
	v_lshl_add_u64 v[62:63], s[6:7], 0, v[58:59]
	v_and_b32_e32 v58, 0xf000, v130
	v_lshl_add_u64 v[34:35], v[60:61], 0, v[26:27]
	v_or_b32_e32 v26, 14, v104
	v_lshl_add_u64 v[64:65], v[62:63], 0, v[58:59]
	v_min_i32_e32 v26, 0xc34f, v26
	global_load_dwordx4 v[72:75], v[64:65], off
	global_load_dwordx4 v[76:79], v[64:65], off offset:512
	v_ashrrev_i32_e32 v27, 31, v26
	v_lshlrev_b64 v[26:27], 9, v[26:27]
	v_lshl_add_u64 v[36:37], v[60:61], 0, v[26:27]
	global_load_dwordx4 v[80:83], v[64:65], off offset:1024
	global_load_dwordx4 v[84:87], v[64:65], off offset:1536
	global_load_dwordx4 v[30:33], v[34:35], off nt
	global_load_dwordx4 v[26:29], v[36:37], off nt
	global_load_dwordx4 v[88:91], v[64:65], off offset:2048
	global_load_dwordx4 v[92:95], v[64:65], off offset:2560
	v_or_b32_e32 v34, 16, v104
	v_min_i32_e32 v34, 0xc34f, v34
	v_or_b32_e32 v36, 18, v104
	v_ashrrev_i32_e32 v35, 31, v34
	v_min_i32_e32 v36, 0xc34f, v36
	global_load_dwordx4 v[96:99], v[64:65], off offset:3072
	global_load_dwordx4 v[100:103], v[64:65], off offset:3584
	v_lshlrev_b64 v[34:35], 9, v[34:35]
	v_ashrrev_i32_e32 v37, 31, v36
	v_lshl_add_u64 v[34:35], v[60:61], 0, v[34:35]
	v_lshlrev_b64 v[36:37], 9, v[36:37]
	v_lshl_add_u64 v[36:37], v[60:61], 0, v[36:37]
	global_load_dwordx4 v[42:45], v[34:35], off nt
	global_load_dwordx4 v[38:41], v[36:37], off nt
	v_or_b32_e32 v34, 20, v104
	v_min_i32_e32 v34, 0xc34f, v34
	v_ashrrev_i32_e32 v35, 31, v34
	v_lshlrev_b64 v[34:35], 9, v[34:35]
	v_lshl_add_u64 v[50:51], v[60:61], 0, v[34:35]
	v_or_b32_e32 v34, 22, v104
	v_min_i32_e32 v34, 0xc34f, v34
	v_ashrrev_i32_e32 v35, 31, v34
	v_lshlrev_b64 v[34:35], 9, v[34:35]
	v_lshl_add_u64 v[52:53], v[60:61], 0, v[34:35]
	global_load_dwordx4 v[46:49], v[50:51], off nt
	global_load_dwordx4 v[34:37], v[52:53], off nt
	v_or_b32_e32 v50, 24, v104
	v_min_i32_e32 v50, 0xc34f, v50
	v_ashrrev_i32_e32 v51, 31, v50
	v_lshlrev_b64 v[50:51], 9, v[50:51]
	v_lshl_add_u64 v[66:67], v[60:61], 0, v[50:51]
	v_or_b32_e32 v50, 26, v104
	v_min_i32_e32 v50, 0xc34f, v50
	s_mov_b32 s3, 0x10000
	v_ashrrev_i32_e32 v51, 31, v50
	v_add_co_u32_e32 v64, vcc, s3, v64
	v_lshlrev_b64 v[50:51], 9, v[50:51]
	v_or_b32_e32 v58, 28, v104
	v_addc_co_u32_e32 v65, vcc, 0, v65, vcc
	v_lshl_add_u64 v[70:71], v[60:61], 0, v[50:51]
	global_load_dwordx4 v[54:57], v[66:67], off nt
	global_load_dwordx4 v[50:53], v[70:71], off nt
	v_min_i32_e32 v66, 0xc34f, v58
	v_or_b32_e32 v58, 30, v104
	global_load_dwordx4 v[104:107], v[64:65], off
	global_load_dwordx4 v[108:111], v[64:65], off offset:512
	v_min_i32_e32 v70, 0xc34f, v58
	global_load_dwordx4 v[112:115], v[64:65], off offset:1024
	global_load_dwordx4 v[116:119], v[64:65], off offset:1536
	global_load_dwordx4 v[120:123], v[64:65], off offset:2048
	global_load_dwordx4 v[124:127], v[64:65], off offset:2560
	v_ashrrev_i32_e32 v67, 31, v66
	v_ashrrev_i32_e32 v71, 31, v70
	s_mov_b32 s3, 0x1fe00
	v_mov_b32_e32 v58, 0x10e00
	v_lshlrev_b64 v[66:67], 9, v[66:67]
	v_lshlrev_b64 v[70:71], 9, v[70:71]
	v_bitop3_b32 v58, v130, s3, v58 bitop3:0xc8
	v_lshl_add_u64 v[66:67], v[60:61], 0, v[66:67]
	v_lshl_add_u64 v[60:61], v[60:61], 0, v[70:71]
	v_lshl_add_u64 v[58:59], v[62:63], 0, v[58:59]
	global_load_dwordx4 v[130:133], v[64:65], off offset:3072
	global_load_dwordx4 v[134:137], v[58:59], off
	s_nop 0
	global_load_dwordx4 v[62:65], v[66:67], off nt
	s_nop 0
	global_load_dwordx4 v[58:61], v[60:61], off nt
	s_mov_b32 s4, 0xbfb8aa3b
	v_lshrrev_b32_e32 v70, 1, v0
	v_and_b32_e32 v71, 0xf0, v70
	s_movk_i32 s3, 0x110
	v_mad_u32_u24 v71, v129, s3, v71
	s_waitcnt vmcnt(25)
	v_mov_b32_e32 v66, v72
	s_waitcnt vmcnt(24)
	v_mov_b32_e32 v67, v76
	v_pk_mul_f32 v[66:67], v[66:67], s[4:5] op_sel_hi:[1,0]
	v_mov_b32_e32 v76, v73
	v_cvt_pk_bf16_f32 v138, v66, v67
	s_waitcnt vmcnt(23)
	v_mov_b32_e32 v66, v80
	s_waitcnt vmcnt(22)
	v_mov_b32_e32 v67, v84
	v_pk_mul_f32 v[66:67], v[66:67], s[4:5] op_sel_hi:[1,0]
	v_mov_b32_e32 v84, v81
	v_cvt_pk_bf16_f32 v139, v66, v67
	s_waitcnt vmcnt(19)
	v_mov_b32_e32 v66, v88
	s_waitcnt vmcnt(18)
	v_mov_b32_e32 v67, v92
	v_pk_mul_f32 v[66:67], v[66:67], s[4:5] op_sel_hi:[1,0]
	v_mov_b32_e32 v92, v89
	v_cvt_pk_bf16_f32 v140, v66, v67
	s_waitcnt vmcnt(17)
	v_mov_b32_e32 v66, v96
	s_waitcnt vmcnt(16)
	v_mov_b32_e32 v67, v100
	v_pk_mul_f32 v[66:67], v[66:67], s[4:5] op_sel_hi:[1,0]
	v_mov_b32_e32 v100, v97
	v_cvt_pk_bf16_f32 v141, v66, v67
	v_pk_mul_f32 v[66:67], v[76:77], s[4:5] op_sel_hi:[1,0]
	ds_write_b128 v71, v[138:141]
	v_cvt_pk_bf16_f32 v138, v66, v67
	v_pk_mul_f32 v[66:67], v[84:85], s[4:5] op_sel_hi:[1,0]
	s_nop 0
	v_cvt_pk_bf16_f32 v139, v66, v67
	v_pk_mul_f32 v[66:67], v[92:93], s[4:5] op_sel_hi:[1,0]
	s_nop 0
	v_cvt_pk_bf16_f32 v140, v66, v67
	v_pk_mul_f32 v[66:67], v[100:101], s[4:5] op_sel_hi:[1,0]
	s_nop 0
	v_cvt_pk_bf16_f32 v141, v66, v67
	v_mov_b32_e32 v66, v74
	v_mov_b32_e32 v67, v78
	v_pk_mul_f32 v[66:67], v[66:67], s[4:5] op_sel_hi:[1,0]
	ds_write_b128 v71, v[138:141] offset:272
	v_cvt_pk_bf16_f32 v138, v66, v67
	v_mov_b32_e32 v66, v82
	v_mov_b32_e32 v67, v86
	v_pk_mul_f32 v[66:67], v[66:67], s[4:5] op_sel_hi:[1,0]
	v_mov_b32_e32 v78, v75
	v_cvt_pk_bf16_f32 v139, v66, v67
	v_mov_b32_e32 v66, v90
	v_mov_b32_e32 v67, v94
	v_pk_mul_f32 v[66:67], v[66:67], s[4:5] op_sel_hi:[1,0]
	v_mov_b32_e32 v86, v83
	v_cvt_pk_bf16_f32 v140, v66, v67
	v_mov_b32_e32 v66, v98
	v_mov_b32_e32 v67, v102
	v_pk_mul_f32 v[66:67], v[66:67], s[4:5] op_sel_hi:[1,0]
	v_mov_b32_e32 v94, v91
	v_cvt_pk_bf16_f32 v141, v66, v67
	v_pk_mul_f32 v[66:67], v[78:79], s[4:5] op_sel_hi:[1,0]
	v_mov_b32_e32 v102, v99
	v_cvt_pk_bf16_f32 v72, v66, v67
	v_pk_mul_f32 v[66:67], v[86:87], s[4:5] op_sel_hi:[1,0]
	ds_write_b128 v71, v[138:141] offset:544
	v_cvt_pk_bf16_f32 v73, v66, v67
	v_pk_mul_f32 v[66:67], v[94:95], s[4:5] op_sel_hi:[1,0]
	s_nop 0
	v_cvt_pk_bf16_f32 v74, v66, v67
	v_pk_mul_f32 v[66:67], v[102:103], s[4:5] op_sel_hi:[1,0]
	s_nop 0
	v_cvt_pk_bf16_f32 v75, v66, v67
	s_waitcnt vmcnt(9)
	v_mov_b32_e32 v66, v104
	s_waitcnt vmcnt(8)
	v_mov_b32_e32 v67, v108
	v_pk_mul_f32 v[66:67], v[66:67], s[4:5] op_sel_hi:[1,0]
	ds_write_b128 v71, v[72:75] offset:816
	v_cvt_pk_bf16_f32 v72, v66, v67
	s_waitcnt vmcnt(7)
	v_mov_b32_e32 v66, v112
	s_waitcnt vmcnt(6)
	v_mov_b32_e32 v67, v116
	v_pk_mul_f32 v[66:67], v[66:67], s[4:5] op_sel_hi:[1,0]
	v_mov_b32_e32 v108, v105
	v_cvt_pk_bf16_f32 v73, v66, v67
	s_waitcnt vmcnt(5)
	v_mov_b32_e32 v66, v120
	s_waitcnt vmcnt(4)
	v_mov_b32_e32 v67, v124
	v_pk_mul_f32 v[66:67], v[66:67], s[4:5] op_sel_hi:[1,0]
	v_mov_b32_e32 v116, v113
	v_cvt_pk_bf16_f32 v74, v66, v67
	s_waitcnt vmcnt(3)
	v_mov_b32_e32 v66, v130
	s_waitcnt vmcnt(2)
	v_mov_b32_e32 v67, v134
	v_pk_mul_f32 v[66:67], v[66:67], s[4:5] op_sel_hi:[1,0]
	v_mov_b32_e32 v124, v121
	v_cvt_pk_bf16_f32 v75, v66, v67
	v_pk_mul_f32 v[66:67], v[108:109], s[4:5] op_sel_hi:[1,0]
	ds_write_b128 v71, v[72:75] offset:34816
	v_cvt_pk_bf16_f32 v72, v66, v67
	v_pk_mul_f32 v[66:67], v[116:117], s[4:5] op_sel_hi:[1,0]
	v_mov_b32_e32 v134, v131
	v_cvt_pk_bf16_f32 v73, v66, v67
	v_pk_mul_f32 v[66:67], v[124:125], s[4:5] op_sel_hi:[1,0]
	s_nop 0
	v_cvt_pk_bf16_f32 v74, v66, v67
	v_pk_mul_f32 v[66:67], v[134:135], s[4:5] op_sel_hi:[1,0]
	s_nop 0
	v_cvt_pk_bf16_f32 v75, v66, v67
	v_mov_b32_e32 v66, v106
	v_mov_b32_e32 v67, v110
	v_pk_mul_f32 v[66:67], v[66:67], s[4:5] op_sel_hi:[1,0]
	ds_write_b128 v71, v[72:75] offset:35088
	v_cvt_pk_bf16_f32 v72, v66, v67
	v_mov_b32_e32 v66, v114
	v_mov_b32_e32 v67, v118
	v_pk_mul_f32 v[66:67], v[66:67], s[4:5] op_sel_hi:[1,0]
	v_mov_b32_e32 v110, v107
	v_cvt_pk_bf16_f32 v73, v66, v67
	v_mov_b32_e32 v66, v122
	v_mov_b32_e32 v67, v126
	v_pk_mul_f32 v[66:67], v[66:67], s[4:5] op_sel_hi:[1,0]
	v_mov_b32_e32 v118, v115
	v_cvt_pk_bf16_f32 v74, v66, v67
	v_mov_b32_e32 v66, v132
	v_mov_b32_e32 v67, v136
	v_pk_mul_f32 v[66:67], v[66:67], s[4:5] op_sel_hi:[1,0]
	v_mov_b32_e32 v126, v123
	v_cvt_pk_bf16_f32 v75, v66, v67
	v_pk_mul_f32 v[66:67], v[110:111], s[4:5] op_sel_hi:[1,0]
	ds_write_b128 v71, v[72:75] offset:35360
	v_cvt_pk_bf16_f32 v72, v66, v67
	v_pk_mul_f32 v[66:67], v[118:119], s[4:5] op_sel_hi:[1,0]
	v_mov_b32_e32 v136, v133
	v_cvt_pk_bf16_f32 v73, v66, v67
	v_pk_mul_f32 v[66:67], v[126:127], s[4:5] op_sel_hi:[1,0]
	s_nop 0
	v_cvt_pk_bf16_f32 v74, v66, v67
	v_pk_mul_f32 v[66:67], v[136:137], s[4:5] op_sel_hi:[1,0]
	s_nop 0
	v_cvt_pk_bf16_f32 v75, v66, v67
	v_lshl_or_b32 v66, s2, 9, v0
	s_movk_i32 s2, 0x2400
	v_cmp_gt_i32_e32 vcc, s2, v66
	v_ashrrev_i32_e32 v67, 7, v66
	ds_write_b128 v71, v[72:75] offset:35632
	s_and_saveexec_b64 s[2:3], vcc
	s_cbranch_execz .LBB0_4
	v_lshlrev_b32_e32 v71, 1, v67
	v_cmp_gt_i32_e32 vcc, 64, v67
	s_and_saveexec_b64 s[4:5], vcc
	v_lshlrev_b32_e32 v72, 3, v67
	v_lshrrev_b32_e32 v73, 7, v66
	v_and_b32_e32 v72, 16, v72
	v_and_b32_e32 v73, 12, v73
	v_and_b32_e32 v71, 0xffffffe2, v71
	v_or3_b32 v71, v72, v73, v71
	s_or_b64 exec, exec, s[4:5]
	v_and_b32_e32 v78, 0x7f, v0
	v_lshl_or_b32 v71, v71, 7, v78
	v_add_u32_e32 v72, 0x8000, v71
	v_ashrrev_i32_e32 v73, 31, v72
	v_add_u32_e32 v74, 0x8080, v71
	v_lshl_add_u64 v[72:73], v[72:73], 2, s[6:7]
	v_ashrrev_i32_e32 v75, 31, v74
	v_lshl_add_u64 v[74:75], v[74:75], 2, s[6:7]
	s_mov_b32 s4, 0xbfb8aa3b
	v_mov_b32_e32 v73, 0
	v_lshlrev_b32_e32 v74, 2, v67
	v_mul_u32_u24_e32 v72, 0x120, v78
	v_ashrrev_i32_e32 v75, 31, v74
	v_lshl_add_u64 v[72:73], s[16:17], 0, v[72:73]
	v_lshl_add_u64 v[72:73], v[72:73], 0, v[74:75]
	v_pk_mul_f32 v[76:77], v[188:189], s[4:5] op_sel_hi:[1,0]
	s_nop 0
	v_cvt_pk_bf16_f32 v71, v76, v77
	global_store_dword v[72:73], v71, off
.LBB0_4:
	s_or_b64 exec, exec, s[2:3]
	s_movk_i32 s2, 0x2000
	v_and_b32_e32 v71, 63, v0
	v_lshrrev_b32_e32 v72, 6, v0
	v_cmp_gt_i32_e32 vcc, s2, v66
	s_and_saveexec_b64 s[2:3], vcc
	s_cbranch_execz .LBB0_6
	v_lshlrev_b32_e32 v74, 8, v67
	v_lshlrev_b32_e32 v75, 10, v67
	v_and_b32_e32 v76, 0x600, v66
	s_movk_i32 s4, 0x800
	v_and_b32_e32 v73, 0x7f, v0
	v_and_or_b32 v75, v75, s4, v76
	v_and_b32_e32 v74, 0xfffff100, v74
	v_or3_b32 v74, v75, v74, v73
	v_ashrrev_i32_e32 v75, 31, v74
	v_lshl_add_u64 v[74:75], v[74:75], 2, s[10:11]
	v_mov_b32_e32 v75, 0
	v_lshlrev_b32_e32 v76, 2, v67
	v_mul_u32_u24_e32 v74, 0x120, v73
	v_ashrrev_i32_e32 v77, 31, v76
	v_lshl_add_u64 v[74:75], s[16:17], 0, v[74:75]
	v_lshl_add_u64 v[74:75], v[74:75], 0, v[76:77]
	v_add_co_u32_e32 v74, vcc, 0x9000, v74
	v_cvt_pk_bf16_f32 v67, v190, v191
	v_addc_co_u32_e32 v75, vcc, 0, v75, vcc
	global_store_dword v[74:75], v67, off
.LBB0_6:
	s_or_b64 exec, exec, s[2:3]
	s_movk_i32 s2, 0x80
	v_cmp_gt_i32_e32 vcc, s2, v66
	s_and_saveexec_b64 s[2:3], vcc
	s_cbranch_execz .LBB0_8
	v_ashrrev_i32_e32 v67, 31, v66
	v_lshlrev_b64 v[66:67], 2, v[66:67]
	s_waitcnt lgkmcnt(0)
	v_lshl_add_u64 v[74:75], s[0:1], 0, v[66:67]
	v_lshl_add_u64 v[66:67], s[16:17], 0, v[66:67]
	v_add_co_u32_e32 v66, vcc, 0x12000, v66
	v_mul_f32_e32 v73, 0xbfb8aa3b, v187
	v_addc_co_u32_e32 v67, vcc, 0, v67, vcc
	global_store_dword v[66:67], v73, off
.LBB0_8:
	s_or_b64 exec, exec, s[2:3]
	v_lshlrev_b32_e32 v129, 1, v69
	v_or_b32_e32 v66, v129, v1
	v_mul_u32_u24_e32 v66, 0x2200, v66
	v_lshlrev_b32_e32 v67, 3, v0
	s_waitcnt lgkmcnt(0)
	s_movk_i32 s0, 0xf8
	v_and_or_b32 v66, v67, s0, v66
	v_cvt_pk_bf16_f32 v6, v6, v7
	v_cvt_pk_bf16_f32 v7, v8, v9
	v_mul_u32_u24_e32 v8, 0x110, v68
	s_mov_b32 s0, 0x11000
	v_add3_u32 v66, v66, v8, s0
	v_cvt_pk_bf16_f32 v2, v2, v3
	v_cvt_pk_bf16_f32 v3, v4, v5
	ds_write2_b64 v66, v[6:7], v[2:3] offset1:68
	v_cvt_pk_bf16_f32 v2, v14, v15
	v_cvt_pk_bf16_f32 v3, v16, v17
	v_cvt_pk_bf16_f32 v4, v10, v11
	v_cvt_pk_bf16_f32 v5, v12, v13
	ds_write2_b64 v66, v[2:3], v[4:5] offset0:136 offset1:204
	v_cvt_pk_bf16_f32 v2, v22, v23
	v_cvt_pk_bf16_f32 v3, v24, v25
	v_cvt_pk_bf16_f32 v4, v18, v19
	v_cvt_pk_bf16_f32 v5, v20, v21
	v_add_u32_e32 v22, 0x800, v66
	ds_write2_b64 v22, v[2:3], v[4:5] offset0:16 offset1:84
	v_cvt_pk_bf16_f32 v2, v30, v31
	v_and_b32_e32 v23, 0x100, v67
	v_cvt_pk_bf16_f32 v3, v32, v33
	v_cvt_pk_bf16_f32 v12, v26, v27
	v_cvt_pk_bf16_f32 v13, v28, v29
	ds_write2_b64 v22, v[2:3], v[12:13] offset0:152 offset1:220
	v_cvt_pk_bf16_f32 v2, v42, v43
	v_cvt_pk_bf16_f32 v3, v44, v45
	v_cvt_pk_bf16_f32 v12, v38, v39
	v_cvt_pk_bf16_f32 v13, v40, v41
	v_add_u32_e32 v22, 0x1000, v66
	ds_write2_b64 v22, v[2:3], v[12:13] offset0:32 offset1:100
	v_cvt_pk_bf16_f32 v2, v46, v47
	v_cvt_pk_bf16_f32 v3, v48, v49
	v_cvt_pk_bf16_f32 v12, v34, v35
	v_cvt_pk_bf16_f32 v13, v36, v37
	ds_write2_b64 v22, v[2:3], v[12:13] offset0:168 offset1:236
	v_cvt_pk_bf16_f32 v2, v54, v55
	v_cvt_pk_bf16_f32 v3, v56, v57
	v_cvt_pk_bf16_f32 v12, v50, v51
	v_cvt_pk_bf16_f32 v13, v52, v53
	v_add_u32_e32 v22, 0x1800, v66
	ds_write2_b64 v22, v[2:3], v[12:13] offset0:48 offset1:116
	s_waitcnt vmcnt(1)
	v_cvt_pk_bf16_f32 v2, v62, v63
	v_cvt_pk_bf16_f32 v3, v64, v65
	s_waitcnt vmcnt(0)
	v_cvt_pk_bf16_f32 v12, v58, v59
	v_cvt_pk_bf16_f32 v13, v60, v61
	ds_write2_b64 v22, v[2:3], v[12:13] offset0:184 offset1:252
	v_lshlrev_b32_e32 v2, 4, v0
	v_and_b32_e32 v3, 64, v2
	v_and_b32_e32 v12, 12, v70
	v_and_b32_e32 v13, 3, v0
	v_or3_b32 v3, v3, v12, v13
	v_and_b32_e32 v130, 31, v0
	v_mul_u32_u24_e32 v3, 0x110, v3
	s_mov_b32 s1, 0x8800
	v_mad_u32_u24 v64, v1, s1, v3
	v_lshlrev_b32_e32 v65, 4, v68
	v_mul_u32_u24_e32 v3, 0x110, v130
	v_add3_u32 v131, v3, v65, s0
	v_mov_b32_e32 v3, 0xbfb8aa3b
	v_cmp_eq_u32_e32 vcc, 0, v1
	s_movk_i32 s0, 0x900
	s_and_b32 s13, s17, 0xffff
	v_cndmask_b32_e32 v50, 0, v3, vcc
	v_mov_b32_e32 v3, 0x22000
	v_mad_u32_u24 v3, v72, s0, v3
	v_and_b32_e32 v2, 0x70, v2
	v_and_b32_e32 v0, 15, v0
	s_movk_i32 s0, 0x90
	v_lshrrev_b32_e32 v134, 3, v71
	v_add_u32_e32 v136, v64, v65
	v_or_b32_e32 v66, v3, v2
	v_mad_u32_u24 v67, v0, s0, v3
	v_lshlrev_b32_e32 v68, 6, v68
	s_add_u32 s6, s16, 0x100000
	v_mul_u32_u24_e32 v69, 0x90, v134
	v_mbcnt_lo_u32_b32 v64, -1, 0
	s_mov_b32 s15, 0x27000
	s_brev_b32 s14, -2
	s_mov_b32 s12, s16
	s_movk_i32 s22, 0x2200
	s_mov_b32 s20, 0
	s_mov_b32 s23, 0xc350
	v_mul_u32_u24_e32 v132, 0xc350, v1
	v_or_b32_e32 v133, 0x200000, v2
	v_cmp_gt_u32_e64 s[0:1], 32, v71
	s_addc_u32 s7, s17, 0
	v_cmp_gt_u32_e64 s[2:3], 16, v130
	v_cmp_lt_u32_e64 s[4:5], 15, v130
	v_or_b32_e32 v135, 8, v134
	s_mov_b64 s[10:11], -1
	s_mov_b64 s[8:9], 0
	s_movk_i32 s24, 0x61b
	s_mov_b32 s25, 0x1e3ce508
	s_mov_b32 s26, 0x42fe0000
	v_mbcnt_hi_u32_b32 v137, -1, v64
	v_add_u32_e32 v138, v67, v68
	v_add_u32_e32 v139, v66, v69
	s_waitcnt vmcnt(14)
	v_pk_mul_f32 v[12:13], v[50:51], v[204:205] op_sel_hi:[0,1]
	v_pk_mul_f32 v[8:9], v[50:51], v[200:201] op_sel_hi:[0,1]
	s_waitcnt vmcnt(12)
	v_pk_mul_f32 v[4:5], v[50:51], v[196:197] op_sel_hi:[0,1]
	v_pk_mul_f32 v[0:1], v[50:51], v[192:193] op_sel_hi:[0,1]
	v_pk_mul_f32 v[14:15], v[50:51], v[206:207] op_sel_hi:[0,1]
	v_pk_mul_f32 v[10:11], v[50:51], v[202:203] op_sel_hi:[0,1]
	v_pk_mul_f32 v[6:7], v[50:51], v[198:199] op_sel_hi:[0,1]
	v_pk_mul_f32 v[2:3], v[50:51], v[194:195] op_sel_hi:[0,1]
	s_waitcnt vmcnt(10)
	v_pk_mul_f32 v[28:29], v[50:51], v[220:221] op_sel_hi:[0,1]
	v_pk_mul_f32 v[24:25], v[50:51], v[216:217] op_sel_hi:[0,1]
	s_waitcnt vmcnt(8)
	v_pk_mul_f32 v[20:21], v[50:51], v[212:213] op_sel_hi:[0,1]
	v_pk_mul_f32 v[16:17], v[50:51], v[208:209] op_sel_hi:[0,1]
	v_pk_mul_f32 v[30:31], v[50:51], v[222:223] op_sel_hi:[0,1]
	v_pk_mul_f32 v[26:27], v[50:51], v[218:219] op_sel_hi:[0,1]
	v_pk_mul_f32 v[22:23], v[50:51], v[214:215] op_sel_hi:[0,1]
	v_pk_mul_f32 v[18:19], v[50:51], v[210:211] op_sel_hi:[0,1]
	s_waitcnt vmcnt(6)
	v_pk_mul_f32 v[44:45], v[50:51], v[236:237] op_sel_hi:[0,1]
	v_pk_mul_f32 v[40:41], v[50:51], v[232:233] op_sel_hi:[0,1]
	s_waitcnt vmcnt(4)
	v_pk_mul_f32 v[36:37], v[50:51], v[228:229] op_sel_hi:[0,1]
	v_pk_mul_f32 v[32:33], v[50:51], v[224:225] op_sel_hi:[0,1]
	v_pk_mul_f32 v[46:47], v[50:51], v[238:239] op_sel_hi:[0,1]
	v_pk_mul_f32 v[42:43], v[50:51], v[234:235] op_sel_hi:[0,1]
	v_pk_mul_f32 v[38:39], v[50:51], v[230:231] op_sel_hi:[0,1]
	v_pk_mul_f32 v[34:35], v[50:51], v[226:227] op_sel_hi:[0,1]
	s_waitcnt vmcnt(2)
	v_pk_mul_f32 v[60:61], v[50:51], v[252:253] op_sel_hi:[0,1]
	v_pk_mul_f32 v[56:57], v[50:51], v[248:249] op_sel_hi:[0,1]
	s_waitcnt vmcnt(0)
	v_pk_mul_f32 v[52:53], v[50:51], v[244:245] op_sel_hi:[0,1]
	v_pk_mul_f32 v[48:49], v[50:51], v[240:241] op_sel_hi:[0,1]
	v_pk_mul_f32 v[62:63], v[50:51], v[254:255] op_sel_hi:[0,1]
	v_pk_mul_f32 v[58:59], v[50:51], v[250:251] op_sel_hi:[0,1]
	v_pk_mul_f32 v[54:55], v[50:51], v[246:247] op_sel_hi:[0,1]
	v_pk_mul_f32 v[50:51], v[50:51], v[242:243] op_sel_hi:[0,1]
	s_waitcnt lgkmcnt(0)
	s_barrier
	s_branch .LBB0_11

.LBB0_11:
	s_cmp_lg_u32 s20, 0
	s_cselect_b64 s[34:35], -1, 0
	v_cndmask_b32_e64 v140, v128, v183, s[34:35]
	v_cmp_gt_i32_e32 vcc, s24, v140
	s_or_b64 s[16:17], s[16:17], exec
	s_and_saveexec_b64 s[18:19], vcc
	s_cbranch_execz .LBB0_10
	v_or_b32_e32 v64, s20, v129
	v_mad_u32_u24 v141, v64, s22, v131
	ds_read_b128 v[142:145], v141
	ds_read_b128 v[146:149], v141 offset:32
	ds_read_b128 v[64:67], v136
	ds_read_b128 v[150:153], v136 offset:32
	ds_read_b128 v[68:71], v136 offset:4352
	ds_read_b128 v[154:157], v136 offset:4384
	ds_read_b128 v[72:75], v136 offset:8704
	ds_read_b128 v[158:161], v136 offset:8736
	ds_read_b128 v[162:165], v136 offset:13056
	ds_read_b128 v[166:169], v136 offset:13088
	s_waitcnt lgkmcnt(7)
	v_mfma_f32_32x32x16_bf16 v[112:127], v[64:67], v[142:145], v[0:15]
	s_waitcnt lgkmcnt(5)
	v_mfma_f32_32x32x16_bf16 v[96:111], v[68:71], v[142:145], v[16:31]
	s_waitcnt lgkmcnt(3)
	v_mfma_f32_32x32x16_bf16 v[80:95], v[72:75], v[142:145], v[32:47]
	s_waitcnt lgkmcnt(1)
	v_mfma_f32_32x32x16_bf16 v[64:79], v[162:165], v[142:145], v[48:63]
	ds_read_b128 v[142:145], v141 offset:64
	ds_read_b128 v[162:165], v136 offset:64
	ds_read_b128 v[170:173], v136 offset:4416
	ds_read_b128 v[174:177], v136 offset:8768
	ds_read_b128 v[178:181], v136 offset:13120
	v_mfma_f32_32x32x16_bf16 v[96:111], v[154:157], v[146:149], v[96:111]
	s_waitcnt lgkmcnt(5)
	v_mfma_f32_32x32x16_bf16 v[64:79], v[166:169], v[146:149], v[64:79]
	v_mfma_f32_32x32x16_bf16 v[112:127], v[150:153], v[146:149], v[112:127]
	v_mfma_f32_32x32x16_bf16 v[80:95], v[158:161], v[146:149], v[80:95]
	ds_read_b128 v[146:149], v141 offset:96
	ds_read_b128 v[150:153], v136 offset:96
	ds_read_b128 v[154:157], v136 offset:4448
	ds_read_b128 v[158:161], v136 offset:8800
	ds_read_b128 v[166:169], v136 offset:13152
	s_waitcnt lgkmcnt(7)
	v_mfma_f32_32x32x16_bf16 v[96:111], v[170:173], v[142:145], v[96:111]
	s_waitcnt lgkmcnt(5)
	v_mfma_f32_32x32x16_bf16 v[64:79], v[178:181], v[142:145], v[64:79]
	v_mfma_f32_32x32x16_bf16 v[112:127], v[162:165], v[142:145], v[112:127]
	v_mfma_f32_32x32x16_bf16 v[80:95], v[174:177], v[142:145], v[80:95]
	ds_read_b128 v[142:145], v141 offset:128
	ds_read_b128 v[162:165], v136 offset:128
	ds_read_b128 v[170:173], v136 offset:4480
	ds_read_b128 v[174:177], v136 offset:8832
	ds_read_b128 v[178:181], v136 offset:13184
	s_waitcnt lgkmcnt(7)
	v_mfma_f32_32x32x16_bf16 v[96:111], v[154:157], v[146:149], v[96:111]
	s_waitcnt lgkmcnt(5)
	v_mfma_f32_32x32x16_bf16 v[64:79], v[166:169], v[146:149], v[64:79]
	v_mfma_f32_32x32x16_bf16 v[112:127], v[150:153], v[146:149], v[112:127]
	v_mfma_f32_32x32x16_bf16 v[80:95], v[158:161], v[146:149], v[80:95]
	ds_read_b128 v[146:149], v141 offset:160
	ds_read_b128 v[150:153], v136 offset:160
	ds_read_b128 v[154:157], v136 offset:4512
	ds_read_b128 v[158:161], v136 offset:8864
	ds_read_b128 v[166:169], v136 offset:13216
	s_waitcnt lgkmcnt(7)
	v_mfma_f32_32x32x16_bf16 v[96:111], v[170:173], v[142:145], v[96:111]
	s_waitcnt lgkmcnt(5)
	v_mfma_f32_32x32x16_bf16 v[64:79], v[178:181], v[142:145], v[64:79]
	v_mfma_f32_32x32x16_bf16 v[112:127], v[162:165], v[142:145], v[112:127]
	v_mfma_f32_32x32x16_bf16 v[80:95], v[174:177], v[142:145], v[80:95]
	ds_read_b128 v[142:145], v141 offset:192
	ds_read_b128 v[162:165], v136 offset:192
	ds_read_b128 v[170:173], v136 offset:4544
	ds_read_b128 v[174:177], v136 offset:8896
	ds_read_b128 v[178:181], v136 offset:13248
	s_waitcnt lgkmcnt(7)
	v_mfma_f32_32x32x16_bf16 v[96:111], v[154:157], v[146:149], v[96:111]
	s_waitcnt lgkmcnt(5)
	v_mfma_f32_32x32x16_bf16 v[64:79], v[166:169], v[146:149], v[64:79]
	v_mfma_f32_32x32x16_bf16 v[112:127], v[150:153], v[146:149], v[112:127]
	v_mfma_f32_32x32x16_bf16 v[80:95], v[158:161], v[146:149], v[80:95]
	ds_read_b128 v[146:149], v141 offset:224
	ds_read_b128 v[150:153], v136 offset:224
	ds_read_b128 v[154:157], v136 offset:4576
	ds_read_b128 v[158:161], v136 offset:8928
	ds_read_b128 v[166:169], v136 offset:13280
	s_waitcnt lgkmcnt(7)
	v_mfma_f32_32x32x16_bf16 v[96:111], v[170:173], v[142:145], v[96:111]
	s_waitcnt lgkmcnt(5)
	v_mfma_f32_32x32x16_bf16 v[64:79], v[178:181], v[142:145], v[64:79]
	v_mfma_f32_32x32x16_bf16 v[112:127], v[162:165], v[142:145], v[112:127]
	v_mfma_f32_32x32x16_bf16 v[80:95], v[174:177], v[142:145], v[80:95]
	s_waitcnt lgkmcnt(2)
	v_mfma_f32_32x32x16_bf16 v[96:111], v[154:157], v[146:149], v[96:111]
	s_waitcnt lgkmcnt(0)
	v_mfma_f32_32x32x16_bf16 v[64:79], v[166:169], v[146:149], v[64:79]
	v_mfma_f32_32x32x16_bf16 v[112:127], v[150:153], v[146:149], v[112:127]
	v_mfma_f32_32x32x16_bf16 v[80:95], v[158:161], v[146:149], v[80:95]
	s_nop 10
	v_max3_f32 v141, |v112|, s25, |v113|
	v_max3_f32 v141, v141, |v114|, |v115|
	v_max3_f32 v141, v141, |v116|, |v117|
	v_max3_f32 v141, v141, |v118|, |v119|
	v_max3_f32 v141, v141, |v120|, |v121|
	v_max3_f32 v141, v141, |v122|, |v123|
	v_max3_f32 v141, v141, |v124|, |v125|
	v_max3_f32 v141, v141, |v126|, |v127|
	v_max3_f32 v141, v141, |v96|, |v97|
	v_max3_f32 v141, v141, |v98|, |v99|
	v_max3_f32 v141, v141, |v100|, |v101|
	v_max3_f32 v141, v141, |v102|, |v103|
	v_max3_f32 v141, v141, |v104|, |v105|
	v_max3_f32 v141, v141, |v106|, |v107|
	v_max3_f32 v141, v141, |v108|, |v109|
	v_max3_f32 v141, v141, |v110|, |v111|
	v_max3_f32 v141, v141, |v80|, |v81|
	v_max3_f32 v141, v141, |v82|, |v83|
	v_max3_f32 v141, v141, |v84|, |v85|
	v_max3_f32 v141, v141, |v86|, |v87|
	v_max3_f32 v141, v141, |v88|, |v89|
	v_max3_f32 v141, v141, |v90|, |v91|
	v_max3_f32 v141, v141, |v92|, |v93|
	v_max3_f32 v141, v141, |v94|, |v95|
	v_max3_f32 v141, v141, |v64|, |v65|
	v_max3_f32 v141, v141, |v66|, |v67|
	v_max3_f32 v141, v141, |v68|, |v69|
	v_max3_f32 v141, v141, |v70|, |v71|
	v_and_b32_e32 v143, 64, v137
	v_max3_f32 v141, v141, |v72|, |v73|
	v_xor_b32_e32 v142, 32, v137
	v_add_u32_e32 v143, 64, v143
	v_max3_f32 v141, v141, |v74|, |v75|
	v_cmp_lt_i32_e32 vcc, v142, v143
	v_max3_f32 v141, v141, |v76|, |v77|
	v_max3_f32 v141, v141, |v78|, |v79|
	v_cndmask_b32_e32 v142, v137, v142, vcc
	v_lshlrev_b32_e32 v142, 2, v142
	ds_bpermute_b32 v142, v142, v141
	s_waitcnt lgkmcnt(0)
	v_max_f32_e32 v142, v142, v142
	v_max_f32_e32 v141, v141, v142
	v_rcp_f32_e32 v142, v141
	s_mov_b32 s30, 0x0c0c0400
	s_mov_b32 s31, 0x04000c0c
	v_mul_f32_e32 v142, 0x42fe0000, v142
	v_fmaak_f32 v216, v112, v142, 0x4b000080
	v_fmaak_f32 v217, v113, v142, 0x4b000080
	v_fmaak_f32 v218, v114, v142, 0x4b000080
	v_fmaak_f32 v219, v115, v142, 0x4b000080
	v_perm_b32 v216, v217, v216, s30
	v_perm_b32 v218, v219, v218, s31
	v_or_b32_e32 v200, v216, v218
	v_fmaak_f32 v220, v96, v142, 0x4b000080
	v_fmaak_f32 v221, v97, v142, 0x4b000080
	v_fmaak_f32 v222, v98, v142, 0x4b000080
	v_fmaak_f32 v223, v99, v142, 0x4b000080
	v_perm_b32 v220, v221, v220, s30
	v_perm_b32 v222, v223, v222, s31
	v_or_b32_e32 v201, v220, v222
	v_fmaak_f32 v216, v80, v142, 0x4b000080
	v_fmaak_f32 v217, v81, v142, 0x4b000080
	v_fmaak_f32 v218, v82, v142, 0x4b000080
	v_fmaak_f32 v219, v83, v142, 0x4b000080
	v_perm_b32 v216, v217, v216, s30
	v_perm_b32 v218, v219, v218, s31
	v_or_b32_e32 v202, v216, v218
	v_fmaak_f32 v220, v64, v142, 0x4b000080
	v_fmaak_f32 v221, v65, v142, 0x4b000080
	v_fmaak_f32 v222, v66, v142, 0x4b000080
	v_fmaak_f32 v223, v67, v142, 0x4b000080
	v_perm_b32 v220, v221, v220, s30
	v_perm_b32 v222, v223, v222, s31
	v_or_b32_e32 v203, v220, v222
	v_fmaak_f32 v216, v116, v142, 0x4b000080
	v_fmaak_f32 v217, v117, v142, 0x4b000080
	v_fmaak_f32 v218, v118, v142, 0x4b000080
	v_fmaak_f32 v219, v119, v142, 0x4b000080
	v_perm_b32 v216, v217, v216, s30
	v_perm_b32 v218, v219, v218, s31
	v_or_b32_e32 v204, v216, v218
	v_fmaak_f32 v220, v100, v142, 0x4b000080
	v_fmaak_f32 v221, v101, v142, 0x4b000080
	v_fmaak_f32 v222, v102, v142, 0x4b000080
	v_fmaak_f32 v223, v103, v142, 0x4b000080
	v_perm_b32 v220, v221, v220, s30
	v_perm_b32 v222, v223, v222, s31
	v_or_b32_e32 v205, v220, v222
	v_fmaak_f32 v216, v84, v142, 0x4b000080
	v_fmaak_f32 v217, v85, v142, 0x4b000080
	v_fmaak_f32 v218, v86, v142, 0x4b000080
	v_fmaak_f32 v219, v87, v142, 0x4b000080
	v_perm_b32 v216, v217, v216, s30
	v_perm_b32 v218, v219, v218, s31
	v_or_b32_e32 v206, v216, v218
	v_fmaak_f32 v220, v68, v142, 0x4b000080
	v_fmaak_f32 v221, v69, v142, 0x4b000080
	v_fmaak_f32 v222, v70, v142, 0x4b000080
	v_fmaak_f32 v223, v71, v142, 0x4b000080
	v_perm_b32 v220, v221, v220, s30
	v_perm_b32 v222, v223, v222, s31
	v_or_b32_e32 v207, v220, v222
	v_fmaak_f32 v216, v120, v142, 0x4b000080
	v_fmaak_f32 v217, v121, v142, 0x4b000080
	v_fmaak_f32 v218, v122, v142, 0x4b000080
	v_fmaak_f32 v219, v123, v142, 0x4b000080
	v_perm_b32 v216, v217, v216, s30
	v_perm_b32 v218, v219, v218, s31
	v_or_b32_e32 v208, v216, v218
	v_fmaak_f32 v220, v104, v142, 0x4b000080
	v_fmaak_f32 v221, v105, v142, 0x4b000080
	v_fmaak_f32 v222, v106, v142, 0x4b000080
	v_fmaak_f32 v223, v107, v142, 0x4b000080
	v_perm_b32 v220, v221, v220, s30
	v_perm_b32 v222, v223, v222, s31
	v_or_b32_e32 v209, v220, v222
	v_fmaak_f32 v216, v88, v142, 0x4b000080
	v_fmaak_f32 v217, v89, v142, 0x4b000080
	v_fmaak_f32 v218, v90, v142, 0x4b000080
	v_fmaak_f32 v219, v91, v142, 0x4b000080
	v_perm_b32 v216, v217, v216, s30
	v_perm_b32 v218, v219, v218, s31
	v_or_b32_e32 v210, v216, v218
	v_fmaak_f32 v220, v72, v142, 0x4b000080
	v_fmaak_f32 v221, v73, v142, 0x4b000080
	v_fmaak_f32 v222, v74, v142, 0x4b000080
	v_fmaak_f32 v223, v75, v142, 0x4b000080
	v_perm_b32 v220, v221, v220, s30
	v_perm_b32 v222, v223, v222, s31
	v_or_b32_e32 v211, v220, v222
	v_fmaak_f32 v216, v124, v142, 0x4b000080
	v_fmaak_f32 v217, v125, v142, 0x4b000080
	v_fmaak_f32 v218, v126, v142, 0x4b000080
	v_fmaak_f32 v219, v127, v142, 0x4b000080
	v_perm_b32 v216, v217, v216, s30
	v_perm_b32 v218, v219, v218, s31
	v_or_b32_e32 v212, v216, v218
	v_fmaak_f32 v220, v108, v142, 0x4b000080
	v_fmaak_f32 v221, v109, v142, 0x4b000080
	v_fmaak_f32 v222, v110, v142, 0x4b000080
	v_fmaak_f32 v223, v111, v142, 0x4b000080
	v_perm_b32 v220, v221, v220, s30
	v_perm_b32 v222, v223, v222, s31
	v_or_b32_e32 v213, v220, v222
	v_fmaak_f32 v216, v92, v142, 0x4b000080
	v_fmaak_f32 v217, v93, v142, 0x4b000080
	v_fmaak_f32 v218, v94, v142, 0x4b000080
	v_fmaak_f32 v219, v95, v142, 0x4b000080
	v_perm_b32 v216, v217, v216, s30
	v_perm_b32 v218, v219, v218, s31
	v_or_b32_e32 v214, v216, v218
	v_fmaak_f32 v220, v76, v142, 0x4b000080
	v_fmaak_f32 v221, v77, v142, 0x4b000080
	v_fmaak_f32 v222, v78, v142, 0x4b000080
	v_fmaak_f32 v223, v79, v142, 0x4b000080
	v_perm_b32 v220, v221, v220, s30
	v_perm_b32 v222, v223, v222, s31
	v_or_b32_e32 v215, v220, v222
	s_and_saveexec_b64 s[20:21], s[2:3]
	s_cbranch_execz .LBB0_14
	ds_write_b128 v138, v[200:203]
	ds_write_b128 v138, v[204:207] offset:16
	ds_write_b128 v138, v[208:211] offset:32
	ds_write_b128 v138, v[212:215] offset:48
.LBB0_14:
	s_or_b64 exec, exec, s[20:21]
	ds_read_b128 v[78:81], v139
	ds_read_b128 v[82:85], v139 offset:1152
	v_lshlrev_b32_e32 v76, 5, v140
	v_or_b32_e32 v77, v134, v76
	v_add_u32_e32 v77, v77, v132
	v_lshl_add_u32 v77, v77, 7, v133
	s_waitcnt lgkmcnt(1)
	buffer_store_dwordx4 v[78:81], v77, s[12:15], 0 offen sc0 sc1
	v_or_b32_e32 v77, v135, v76
	v_add_u32_e32 v77, v77, v132
	v_lshl_add_u32 v77, v77, 7, v133
	s_waitcnt lgkmcnt(0)
	buffer_store_dwordx4 v[82:85], v77, s[12:15], 0 offen sc0 sc1
	s_and_saveexec_b64 s[20:21], s[4:5]
	s_cbranch_execz .LBB0_16
	ds_write_b128 v138, v[200:203]
	ds_write_b128 v138, v[204:207] offset:16
	ds_write_b128 v138, v[208:211] offset:32
	ds_write_b128 v138, v[212:215] offset:48

	.amdhsa_kernel _Z4prepPKfS0_S0_S0_S0_Pc
		.amdhsa_group_segment_fixed_size 157696
		.amdhsa_private_segment_fixed_size 0
		.amdhsa_kernarg_size 48
		.amdhsa_user_sgpr_count 2
		.amdhsa_user_sgpr_dispatch_ptr 0
		.amdhsa_user_sgpr_queue_ptr 0
		.amdhsa_user_sgpr_kernarg_segment_ptr 1
		.amdhsa_user_sgpr_dispatch_id 0
		.amdhsa_user_sgpr_kernarg_preload_length 0
		.amdhsa_user_sgpr_kernarg_preload_offset 0
		.amdhsa_user_sgpr_private_segment_size 0
		.amdhsa_uses_dynamic_stack 0
		.amdhsa_enable_private_segment 0
		.amdhsa_system_sgpr_workgroup_id_x 1
		.amdhsa_system_sgpr_workgroup_id_y 0
		.amdhsa_system_sgpr_workgroup_id_z 0
		.amdhsa_system_sgpr_workgroup_info 0
		.amdhsa_system_vgpr_workitem_id 0
		.amdhsa_next_free_vgpr 256
		.amdhsa_next_free_sgpr 96
		.amdhsa_accum_offset 256
		.amdhsa_reserve_vcc 1
		.amdhsa_float_round_mode_32 0
		.amdhsa_float_round_mode_16_64 0
		.amdhsa_float_denorm_mode_32 3
		.amdhsa_float_denorm_mode_16_64 3
		.amdhsa_dx10_clamp 1
		.amdhsa_ieee_mode 1
		.amdhsa_fp16_overflow 0
		.amdhsa_tg_split 0
		.amdhsa_exception_fp_ieee_invalid_op 0
		.amdhsa_exception_fp_denorm_src 0
		.amdhsa_exception_fp_ieee_div_zero 0
		.amdhsa_exception_fp_ieee_overflow 0
		.amdhsa_exception_fp_ieee_underflow 0
		.amdhsa_exception_fp_ieee_inexact 0
		.amdhsa_exception_int_div_zero 0
	.end_amdhsa_kernel

amdhsa.kernels:
  - .agpr_count:     0
    .args:
      - .actual_access:  read_only
        .address_space:  global
        .offset:         0
        .size:           8
        .value_kind:     global_buffer
      - .actual_access:  read_only
        .address_space:  global
        .offset:         8
        .size:           8
        .value_kind:     global_buffer
      - .actual_access:  read_only
        .address_space:  global
        .offset:         16
        .size:           8
        .value_kind:     global_buffer
      - .actual_access:  read_only
        .address_space:  global
        .offset:         24
        .size:           8
        .value_kind:     global_buffer
      - .actual_access:  read_only
        .address_space:  global
        .offset:         32
        .size:           8
        .value_kind:     global_buffer
      - .actual_access:  write_only
        .address_space:  global
        .offset:         40
        .size:           8
        .value_kind:     global_buffer
    .group_segment_fixed_size: 157696
    .kernarg_segment_align: 8
    .kernarg_segment_size: 48
    .language:       OpenCL C
    .language_version:
      - 2
      - 0
    .max_flat_workgroup_size: 512
    .name:           _Z4prepPKfS0_S0_S0_S0_Pc
    .private_segment_fixed_size: 0
    .sgpr_count:     36
    .sgpr_spill_count: 0
    .symbol:         _Z4prepPKfS0_S0_S0_S0_Pc.kd
    .uniform_work_group_size: 1
    .uses_dynamic_stack: false
    .vgpr_count:     256
    .vgpr_spill_count: 0
    .wavefront_size: 64
  - .agpr_count:     0
    .args:
      - .actual_access:  read_only
        .address_space:  global
        .offset:         0
        .size:           8
        .value_kind:     global_buffer
      - .actual_access:  read_only
        .address_space:  global
        .offset:         8
        .size:           8
        .value_kind:     global_buffer
      - .actual_access:  read_only
        .address_space:  global
        .offset:         16
        .size:           8
        .value_kind:     global_buffer
      - .actual_access:  read_only
        .address_space:  global
        .offset:         24
        .size:           8
        .value_kind:     global_buffer
      - .actual_access:  read_only
        .address_space:  global
        .offset:         32
        .size:           8
        .value_kind:     global_buffer
      - .actual_access:  write_only
        .address_space:  global
        .offset:         40
        .size:           8
        .value_kind:     global_buffer
      - .actual_access:  read_only
        .address_space:  global
        .offset:         48
        .size:           8
        .value_kind:     global_buffer
      - .actual_access:  read_only
        .address_space:  global
        .offset:         56
        .size:           8
        .value_kind:     global_buffer
      - .actual_access:  write_only
        .address_space:  global
        .offset:         64
        .size:           8
        .value_kind:     global_buffer
    .group_segment_fixed_size: 156160
    .kernarg_segment_align: 8
    .kernarg_segment_size: 72
    .language:       OpenCL C
    .language_version:
      - 2
      - 0
    .max_flat_workgroup_size: 512
    .name:           _Z9edge_mainPKfS0_PKiS2_PKcPcS0_S0_Pf
    .private_segment_fixed_size: 0
    .sgpr_count:     22
    .sgpr_spill_count: 0
    .symbol:         _Z9edge_mainPKfS0_PKiS2_PKcPcS0_S0_Pf.kd
    .uniform_work_group_size: 1
    .uses_dynamic_stack: false
    .vgpr_count:     236
    .vgpr_spill_count: 0
    .wavefront_size: 64
